# speedup vs baseline: 1.0161x; 1.0161x over previous
.LBB5_6:
	s_or_b64 exec, exec, s[10:11]
	s_load_dwordx2 s[10:11], s[0:1], 0x80
	s_load_dwordx2 s[36:37], s[0:1], 0x70
	s_load_dwordx2 s[40:41], s[0:1], 0x60
	s_load_dwordx4 s[20:23], s[0:1], 0x50
	s_load_dwordx8 s[12:19], s[0:1], 0x30
	s_load_dwordx4 s[24:27], s[0:1], 0x10
	s_load_dwordx2 s[46:47], s[0:1], 0x20
	s_and_b32 s58, s59, 1
	s_cmp_eq_u32 s35, 0
	s_cselect_b32 s42, s3, s7
	s_ashr_i32 s7, s6, 31
	s_lshl_b64 s[52:53], s[6:7], 22
	s_waitcnt lgkmcnt(0)
	v_readfirstlane_b32 s64, v0
	s_lshr_b32 s64, s64, 6
	s_cmp_gt_u32 s64, 3
	s_cbranch_scc1 .Lstash_done
	s_cmp_eq_u32 s64, 1
	s_cselect_b32 s66, s12, s14
	s_cselect_b32 s67, s13, s15
	s_cmp_eq_u32 s64, 3
	s_cselect_b32 s66, s16, s66
	s_cselect_b32 s67, s17, s67
	s_lshl_b32 s65, s42, 10
	s_cmp_eq_u32 s64, 0
	s_cselect_b32 s66, s24, s66
	s_cselect_b32 s67, s25, s67
	s_cbranch_scc0 .Lstash_off
	s_lshl_b32 s65, s42, 11
	s_lshl_b32 s68, s58, 10
	s_add_u32 s65, s65, s68
.Lstash_off:
	s_add_u32 s66, s66, s65
	s_addc_u32 s67, s67, 0
	s_lshl_b32 s68, s64, 10
	s_add_i32 s68, s68, 0x22240
	s_mov_b32 m0, s68
	v_and_b32_e32 v254, 63, v0
	v_lshlrev_b32_e32 v254, 4, v254
	global_load_lds_dwordx4 v254, s[66:67]
.Lstash_done:
	s_lshl_b32 s65, s42, 2
	s_load_dword s69, s[18:19], s65
	s_add_u32 s3, s28, s52
	s_addc_u32 s7, s29, s53
	s_lshl_b32 s35, s33, 19
	s_and_b32 s35, s35, 0x300000
	s_add_u32 s50, s3, s35
	s_addc_u32 s51, s7, 0
	s_ashr_i32 s43, s42, 31
	s_lshl_b32 s7, s58, 8
	s_lshl_b64 s[54:55], s[42:43], 21
	v_lshlrev_b32_e32 v162, 4, v0
	v_and_b32_e32 v2, 32, v0
	s_add_u32 s35, s30, s54
	v_bitop3_b32 v12, v162, v2, 48 bitop3:0x6c
	v_and_b32_e32 v13, 64, v0
	s_addc_u32 s38, s31, s55
	s_lshl_b32 s3, s58, 20
	v_lshrrev_b32_e32 v4, 3, v0
	v_bfe_u32 v3, v0, 2, 4
	v_or_b32_e32 v2, v12, v13
	v_or_b32_e32 v164, 0x2000, v162
	s_add_u32 s56, s35, s3
	v_and_or_b32 v4, v4, 48, v3
	v_lshrrev_b32_e32 v2, 1, v2
	v_lshrrev_b32_e32 v5, 7, v164
	s_movk_i32 s35, 0x70
	v_add_u32_e32 v142, 0, v162
	v_lshl_or_b32 v4, v4, 11, v2
	v_and_or_b32 v5, v5, s35, v3
	v_readfirstlane_b32 s35, v142
	v_add_u32_e32 v143, 0x2000, v142
	v_lshlrev_b32_e32 v130, 1, v4
	s_mov_b32 m0, s35
	v_readfirstlane_b32 s35, v143
	s_addc_u32 s57, s38, 0
	s_mov_b32 m0, s35
	s_add_i32 s35, 0, 0x10000
	v_lshl_or_b32 v2, v5, 11, v2
	v_add_u32_e32 v144, s35, v162
	v_lshlrev_b32_e32 v132, 1, v2
	v_readfirstlane_b32 s38, v144
	v_add_u32_e32 v145, 0x2000, v144
	s_mov_b32 m0, s38
	v_readfirstlane_b32 s38, v145
	v_add_u32_e32 v151, 0x4000, v142
	global_load_lds_dwordx4 v130, s[56:57]
	s_mov_b32 m0, s38
	s_add_u32 s38, s50, 0x80000
	v_readfirstlane_b32 s44, v151
	v_add_u32_e32 v153, 0x6000, v142
	global_load_lds_dwordx4 v132, s[56:57]
	s_addc_u32 s39, s51, 0
	s_mov_b32 m0, s44
	v_readfirstlane_b32 s44, v153
	s_mov_b32 m0, s44
	v_mov_b32_e32 v2, 0
	s_add_u32 s38, s56, 0x80000
	s_addc_u32 s39, s57, 0
	s_add_i32 s60, 0, 0x14000
	v_add_u32_e32 v154, s60, v162
	v_add_u32_e32 v155, 0x2000, v154
	v_readfirstlane_b32 s44, v154
	s_mov_b32 m0, s44
	v_readfirstlane_b32 s44, v155
	global_load_lds_dwordx4 v130, s[38:39]
	s_mov_b32 m0, s44
	v_lshrrev_b32_e32 v14, 8, v0
	global_load_lds_dwordx4 v132, s[38:39]
	v_mov_b32_e32 v131, v2
	v_mov_b32_e32 v133, v2
	v_lshl_add_u64 v[10:11], s[50:51], 0, v[130:131]
	v_lshl_add_u64 v[8:9], s[50:51], 0, v[132:133]
	v_lshl_add_u64 v[6:7], s[56:57], 0, v[130:131]
	v_lshl_add_u64 v[4:5], s[56:57], 0, v[132:133]
	v_cmp_eq_u32_e32 vcc, 1, v14
	s_and_saveexec_b64 s[38:39], vcc
	s_cbranch_execz .LBB5_8
	s_barrier
